# flat-release barrier + first local arriver of each XCD issues an early non-blocking buffer_wbl2 (starts the L2 write-back while stragglers finish)
# baseline (speedup 1.0000x reference)
.LBB0_69:
	s_lshl_b32 s4, s33, 8
	s_add_u32 s4, s14, s4
	s_addc_u32 s5, s15, 0
	v_mov_b32_e32 v2, 0x1000
	v_mov_b32_e32 v4, 1
	global_atomic_add v4, v2, v4, s[4:5] offset:1024 sc0
	buffer_inv sc1
	v_cvt_f32_u32_e32 v2, v3
	v_sub_u32_e32 v5, 0, v3
	v_rcp_iflag_f32_e32 v2, v2
	s_nop 0
	v_mul_f32_e32 v2, 0x4f7ffffe, v2
	v_cvt_u32_f32_e32 v2, v2
	v_mul_lo_u32 v5, v5, v2
	v_mul_hi_u32 v5, v2, v5
	v_add_u32_e32 v2, v2, v5
	s_waitcnt vmcnt(1)
	v_mul_hi_u32 v2, v4, v2
	v_mul_lo_u32 v5, v2, v3
	v_sub_u32_e32 v5, v4, v5
	v_add_u32_e32 v6, 1, v2
	v_cmp_ge_u32_e32 vcc, v5, v3
	v_add_u32_e32 v4, 1, v4
	s_nop 0
	v_cndmask_b32_e32 v2, v2, v6, vcc
	v_sub_u32_e32 v6, v5, v3
	v_cndmask_b32_e32 v5, v5, v6, vcc
	v_add_u32_e32 v6, 1, v2
	v_cmp_ge_u32_e32 vcc, v5, v3
	s_nop 1
	v_cndmask_b32_e32 v2, v2, v6, vcc
	v_mul_lo_u32 v5, v3, v2
	v_add_u32_e32 v3, v5, v3
	v_cmp_ne_u32_e32 vcc, v4, v3
	v_sub_u32_e32 v6, v3, v5
	s_waitcnt lgkmcnt(0)
	v_mov_b32_e32 v1, 0
	v_add_u32_e32 v7, 1, v5
	v_cmp_eq_u32_e64 s[22:23], v4, v7
	v_add_u32_e32 v2, 1, v2
	v_lshlrev_b32_e32 v2, 8, v2
	s_add_u32 s8, s4, 0x2400
	s_addc_u32 s9, s5, 0
	s_waitcnt lgkmcnt(0)
	s_cbranch_vccnz .Lnb_nl_99
	buffer_wbl2 sc1
	s_add_u32 s12, s16, 0x6400
	s_addc_u32 s13, s17, 0
	s_mov_b32 s10, 16
	s_waitcnt vmcnt(0)
.Lnb_loop_99:
	global_atomic_add v1, v6, s[12:13]
	s_add_u32 s12, s12, 0x100
	s_addc_u32 s13, s13, 0
	s_sub_u32 s10, s10, 1
	s_cmp_lg_u32 s10, 0
	s_cbranch_scc1 .Lnb_loop_99
	s_branch .Lnb_poll_99
.Lnb_nl_99:
	s_cmp_eq_u64 s[22:23], 0
	s_cbranch_scc1 .Lnb_poll_99
	buffer_wbl2 sc1

.LBB0_170:
	v_readlane_b32 s4, v253, 8
	v_readlane_b32 s5, v253, 9
	v_cvt_f32_u32_e32 v1, v4
	v_sub_u32_e32 v6, 0, v4
	v_rcp_iflag_f32_e32 v1, v1
	s_nop 1
	global_atomic_add v5, v3, v228, s[4:5] sc0
	buffer_inv sc1
	v_mul_f32_e32 v1, 0x4f7ffffe, v1
	v_cvt_u32_f32_e32 v1, v1
	v_mul_lo_u32 v6, v6, v1
	v_mul_hi_u32 v6, v1, v6
	v_add_u32_e32 v1, v1, v6
	s_waitcnt vmcnt(1)
	v_mul_hi_u32 v1, v5, v1
	v_mul_lo_u32 v6, v1, v4
	v_sub_u32_e32 v6, v5, v6
	v_add_u32_e32 v7, 1, v1
	v_cmp_ge_u32_e32 vcc, v6, v4
	v_add_u32_e32 v5, 1, v5
	s_nop 0
	v_cndmask_b32_e32 v1, v1, v7, vcc
	v_sub_u32_e32 v7, v6, v4
	v_cndmask_b32_e32 v6, v6, v7, vcc
	v_add_u32_e32 v7, 1, v1
	v_cmp_ge_u32_e32 vcc, v6, v4
	s_nop 1
	v_cndmask_b32_e32 v1, v1, v7, vcc
	v_mul_lo_u32 v6, v4, v1
	v_add_u32_e32 v4, v6, v4
	v_cmp_ne_u32_e32 vcc, v5, v4
	v_sub_u32_e32 v7, v4, v6
	v_add_u32_e32 v8, 1, v6
	v_cmp_eq_u32_e64 s[38:39], v5, v8
	v_add_u32_e32 v1, 1, v1
	v_lshlrev_b32_e32 v1, 8, v1
	v_readlane_b32 s6, v253, 10
	v_readlane_b32 s7, v253, 11
	s_waitcnt lgkmcnt(0)
	s_cbranch_vccnz .Lnb_nl_0
	buffer_wbl2 sc1
	s_add_u32 s12, s16, 0x6400
	s_addc_u32 s13, s17, 0
	s_mov_b32 s14, 16
	s_waitcnt vmcnt(0)
.Lnb_loop_0:
	global_atomic_add v3, v7, s[12:13]
	s_add_u32 s12, s12, 0x100
	s_addc_u32 s13, s13, 0
	s_sub_u32 s14, s14, 1
	s_cmp_lg_u32 s14, 0
	s_cbranch_scc1 .Lnb_loop_0
	s_branch .Lnb_poll_0
.Lnb_nl_0:
	s_cmp_eq_u64 s[38:39], 0
	s_cbranch_scc1 .Lnb_poll_0
	buffer_wbl2 sc1
